# MoE phase start: row-block to expert lookup rewritten (64 serialized LDS round trips replaced by 16 wide reads and a branch-free compare chain)
# speedup vs baseline: 1.0049x; 1.0049x over previous
.LBB0_1935:
	s_mov_b64 s[10:11], exec
	v_mov_b32_e32 v6, 0x20080
	ds_read_b128 v[56:59], v6
	ds_read_b128 v[60:63], v6 offset:16
	ds_read_b128 v[64:67], v6 offset:32
	ds_read_b128 v[68:71], v6 offset:48
	ds_read_b128 v[72:75], v6 offset:64
	ds_read_b128 v[76:79], v6 offset:80
	ds_read_b128 v[80:83], v6 offset:96
	ds_read_b128 v[84:87], v6 offset:112
	ds_read_b128 v[88:91], v6 offset:128
	ds_read_b128 v[92:95], v6 offset:144
	ds_read_b128 v[96:99], v6 offset:160
	ds_read_b128 v[100:103], v6 offset:176
	ds_read_b128 v[104:107], v6 offset:192
	ds_read_b128 v[108:111], v6 offset:208
	ds_read_b128 v[112:115], v6 offset:224
	ds_read_b128 v[116:119], v6 offset:240
	v_mov_b32_e32 v5, -1
	s_waitcnt lgkmcnt(0)
	v_cmp_ge_i32_e32 vcc, v3, v56
	v_cmp_lt_i32_e64 s[12:13], v3, v88
	s_and_b64 vcc, vcc, s[12:13]
	v_cndmask_b32_e64 v5, v5, 0, vcc
	v_cmp_ge_i32_e32 vcc, v3, v57
	v_cmp_lt_i32_e64 s[12:13], v3, v89
	s_and_b64 vcc, vcc, s[12:13]
	v_cndmask_b32_e64 v5, v5, 1, vcc
	v_cmp_ge_i32_e32 vcc, v3, v58
	v_cmp_lt_i32_e64 s[12:13], v3, v90
	s_and_b64 vcc, vcc, s[12:13]
	v_cndmask_b32_e64 v5, v5, 2, vcc
	v_cmp_ge_i32_e32 vcc, v3, v59
	v_cmp_lt_i32_e64 s[12:13], v3, v91
	s_and_b64 vcc, vcc, s[12:13]
	v_cndmask_b32_e64 v5, v5, 3, vcc
	v_cmp_ge_i32_e32 vcc, v3, v60
	v_cmp_lt_i32_e64 s[12:13], v3, v92
	s_and_b64 vcc, vcc, s[12:13]
	v_cndmask_b32_e64 v5, v5, 4, vcc
	v_cmp_ge_i32_e32 vcc, v3, v61
	v_cmp_lt_i32_e64 s[12:13], v3, v93
	s_and_b64 vcc, vcc, s[12:13]
	v_cndmask_b32_e64 v5, v5, 5, vcc
	v_cmp_ge_i32_e32 vcc, v3, v62
	v_cmp_lt_i32_e64 s[12:13], v3, v94
	s_and_b64 vcc, vcc, s[12:13]
	v_cndmask_b32_e64 v5, v5, 6, vcc
	v_cmp_ge_i32_e32 vcc, v3, v63
	v_cmp_lt_i32_e64 s[12:13], v3, v95
	s_and_b64 vcc, vcc, s[12:13]
	v_cndmask_b32_e64 v5, v5, 7, vcc
	v_cmp_ge_i32_e32 vcc, v3, v64
	v_cmp_lt_i32_e64 s[12:13], v3, v96
	s_and_b64 vcc, vcc, s[12:13]
	v_cndmask_b32_e64 v5, v5, 8, vcc
	v_cmp_ge_i32_e32 vcc, v3, v65
	v_cmp_lt_i32_e64 s[12:13], v3, v97
	s_and_b64 vcc, vcc, s[12:13]
	v_cndmask_b32_e64 v5, v5, 9, vcc
	v_cmp_ge_i32_e32 vcc, v3, v66
	v_cmp_lt_i32_e64 s[12:13], v3, v98
	s_and_b64 vcc, vcc, s[12:13]
	v_cndmask_b32_e64 v5, v5, 10, vcc
	v_cmp_ge_i32_e32 vcc, v3, v67
	v_cmp_lt_i32_e64 s[12:13], v3, v99
	s_and_b64 vcc, vcc, s[12:13]
	v_cndmask_b32_e64 v5, v5, 11, vcc
	v_cmp_ge_i32_e32 vcc, v3, v68
	v_cmp_lt_i32_e64 s[12:13], v3, v100
	s_and_b64 vcc, vcc, s[12:13]
	v_cndmask_b32_e64 v5, v5, 12, vcc
	v_cmp_ge_i32_e32 vcc, v3, v69
	v_cmp_lt_i32_e64 s[12:13], v3, v101
	s_and_b64 vcc, vcc, s[12:13]
	v_cndmask_b32_e64 v5, v5, 13, vcc
	v_cmp_ge_i32_e32 vcc, v3, v70
	v_cmp_lt_i32_e64 s[12:13], v3, v102
	s_and_b64 vcc, vcc, s[12:13]
	v_cndmask_b32_e64 v5, v5, 14, vcc
	v_cmp_ge_i32_e32 vcc, v3, v71
	v_cmp_lt_i32_e64 s[12:13], v3, v103
	s_and_b64 vcc, vcc, s[12:13]
	v_cndmask_b32_e64 v5, v5, 15, vcc
	v_cmp_ge_i32_e32 vcc, v3, v72
	v_cmp_lt_i32_e64 s[12:13], v3, v104
	s_and_b64 vcc, vcc, s[12:13]
	v_cndmask_b32_e64 v5, v5, 16, vcc
	v_cmp_ge_i32_e32 vcc, v3, v73
	v_cmp_lt_i32_e64 s[12:13], v3, v105
	s_and_b64 vcc, vcc, s[12:13]
	v_cndmask_b32_e64 v5, v5, 17, vcc
	v_cmp_ge_i32_e32 vcc, v3, v74
	v_cmp_lt_i32_e64 s[12:13], v3, v106
	s_and_b64 vcc, vcc, s[12:13]
	v_cndmask_b32_e64 v5, v5, 18, vcc
	v_cmp_ge_i32_e32 vcc, v3, v75
	v_cmp_lt_i32_e64 s[12:13], v3, v107
	s_and_b64 vcc, vcc, s[12:13]
	v_cndmask_b32_e64 v5, v5, 19, vcc
	v_cmp_ge_i32_e32 vcc, v3, v76
	v_cmp_lt_i32_e64 s[12:13], v3, v108
	s_and_b64 vcc, vcc, s[12:13]
	v_cndmask_b32_e64 v5, v5, 20, vcc
	v_cmp_ge_i32_e32 vcc, v3, v77
	v_cmp_lt_i32_e64 s[12:13], v3, v109
	s_and_b64 vcc, vcc, s[12:13]
	v_cndmask_b32_e64 v5, v5, 21, vcc
	v_cmp_ge_i32_e32 vcc, v3, v78
	v_cmp_lt_i32_e64 s[12:13], v3, v110
	s_and_b64 vcc, vcc, s[12:13]
	v_cndmask_b32_e64 v5, v5, 22, vcc
	v_cmp_ge_i32_e32 vcc, v3, v79
	v_cmp_lt_i32_e64 s[12:13], v3, v111
	s_and_b64 vcc, vcc, s[12:13]
	v_cndmask_b32_e64 v5, v5, 23, vcc
	v_cmp_ge_i32_e32 vcc, v3, v80
	v_cmp_lt_i32_e64 s[12:13], v3, v112
	s_and_b64 vcc, vcc, s[12:13]
	v_cndmask_b32_e64 v5, v5, 24, vcc
	v_cmp_ge_i32_e32 vcc, v3, v81
	v_cmp_lt_i32_e64 s[12:13], v3, v113
	s_and_b64 vcc, vcc, s[12:13]
	v_cndmask_b32_e64 v5, v5, 25, vcc
	v_cmp_ge_i32_e32 vcc, v3, v82
	v_cmp_lt_i32_e64 s[12:13], v3, v114
	s_and_b64 vcc, vcc, s[12:13]
	v_cndmask_b32_e64 v5, v5, 26, vcc
	v_cmp_ge_i32_e32 vcc, v3, v83
	v_cmp_lt_i32_e64 s[12:13], v3, v115
	s_and_b64 vcc, vcc, s[12:13]
	v_cndmask_b32_e64 v5, v5, 27, vcc
	v_cmp_ge_i32_e32 vcc, v3, v84
	v_cmp_lt_i32_e64 s[12:13], v3, v116
	s_and_b64 vcc, vcc, s[12:13]
	v_cndmask_b32_e64 v5, v5, 28, vcc
	v_cmp_ge_i32_e32 vcc, v3, v85
	v_cmp_lt_i32_e64 s[12:13], v3, v117
	s_and_b64 vcc, vcc, s[12:13]
	v_cndmask_b32_e64 v5, v5, 29, vcc
	v_cmp_ge_i32_e32 vcc, v3, v86
	v_cmp_lt_i32_e64 s[12:13], v3, v118
	s_and_b64 vcc, vcc, s[12:13]
	v_cndmask_b32_e64 v5, v5, 30, vcc
	v_cmp_ge_i32_e32 vcc, v3, v87
	v_cmp_lt_i32_e64 s[12:13], v3, v119
	s_and_b64 vcc, vcc, s[12:13]
	v_cndmask_b32_e64 v5, v5, 31, vcc
	s_branch .LBB0_1934
